# strategy: one static s_setprio 1 for the younger wave half (waves 4-7) during the attention phase, reset to 0 at its end; on top of the gla_gates pool and first-barrier census batch
# speedup vs baseline: 1.0059x; 1.0054x over previous
.LBB0_259:
	v_readlane_b32 s100, v252, 5
	s_cmp_ge_u32 s100, 4
	s_cbranch_scc0 .Lattn_prio_done
	s_setprio 1

.LBB0_283:
	s_setprio 0
	v_mbcnt_lo_u32_b32 v142, -1, 0
	v_mbcnt_hi_u32_b32 v142, -1, v142
	v_readlane_b32 s4, v252, 10
	s_nop 1
	v_add_u32_e32 v178, s4, v142
